# speedup vs baseline: 1.0140x; 1.0140x over previous
_Z13logits_kernelPKDv8_DF16bS1_PKfS3_PDv2_fS5_Pf:
	s_load_dwordx4 s[4:7], s[0:1], 0x0
	s_load_dwordx4 s[12:15], s[0:1], 0x10
	s_lshl_b32 s3, s2, 1
	s_and_b32 s3, s3, 14
	s_ashr_i32 s8, s2, 7
	s_bfe_u32 s10, s2, 0x40003
	s_add_i32 s3, s3, s8
	v_lshrrev_b32_e32 v1, 6, v0
	v_and_b32_e32 v2, 63, v0
	s_movk_i32 s11, 0x3000
	v_lshlrev_b32_e32 v2, 4, v2
	v_and_b32_e32 v5, 31, v0
	v_mad_u32_u24 v2, v1, s11, v2
	v_lshlrev_b32_e32 v5, 2, v5
	s_lshl_b32 s9, s3, 9
	v_add_u32_e32 v3, 0x1000, v2
	v_add_u32_e32 v4, 0x2000, v2
	v_add_u32_e32 v5, s9, v5
	s_mul_i32 s8, s10, 0xc000
	s_mul_i32 s9, s3, 0x30000
	s_waitcnt lgkmcnt(0)
	s_load_dword s22, s[14:15], 0x0
	global_load_dword v248, v5, s[12:13]
	global_load_dword v249, v5, s[12:13] offset:128
	global_load_dword v250, v5, s[12:13] offset:256
	global_load_dword v251, v5, s[12:13] offset:384
	s_add_u32 s4, s4, s8
	s_addc_u32 s5, s5, 0
	s_add_u32 s6, s6, s9
	s_addc_u32 s7, s7, 0
	s_add_u32 s16, s6, 0xc000
	s_addc_u32 s17, s7, 0
	s_add_u32 s18, s6, 0x18000
	s_addc_u32 s19, s7, 0
	s_add_u32 s20, s6, 0x24000
	s_addc_u32 s21, s7, 0
	global_load_dwordx4 v[8:11], v2, s[4:5]
	global_load_dwordx4 v[56:59], v2, s[6:7]
	global_load_dwordx4 v[104:107], v2, s[16:17]
	global_load_dwordx4 v[152:155], v2, s[18:19]
	global_load_dwordx4 v[200:203], v2, s[20:21]
	global_load_dwordx4 v[12:15], v2, s[4:5] offset:1024
	global_load_dwordx4 v[60:63], v2, s[6:7] offset:1024
	global_load_dwordx4 v[108:111], v2, s[16:17] offset:1024
	global_load_dwordx4 v[156:159], v2, s[18:19] offset:1024
	global_load_dwordx4 v[204:207], v2, s[20:21] offset:1024
	global_load_dwordx4 v[16:19], v2, s[4:5] offset:2048
	global_load_dwordx4 v[64:67], v2, s[6:7] offset:2048
	global_load_dwordx4 v[112:115], v2, s[16:17] offset:2048
	global_load_dwordx4 v[160:163], v2, s[18:19] offset:2048
	global_load_dwordx4 v[208:211], v2, s[20:21] offset:2048
	global_load_dwordx4 v[20:23], v2, s[4:5] offset:3072
	global_load_dwordx4 v[68:71], v2, s[6:7] offset:3072
	global_load_dwordx4 v[116:119], v2, s[16:17] offset:3072
	global_load_dwordx4 v[164:167], v2, s[18:19] offset:3072
	global_load_dwordx4 v[212:215], v2, s[20:21] offset:3072
	global_load_dwordx4 v[24:27], v3, s[4:5]
	global_load_dwordx4 v[72:75], v3, s[6:7]
	global_load_dwordx4 v[120:123], v3, s[16:17]
	global_load_dwordx4 v[168:171], v3, s[18:19]
	global_load_dwordx4 v[216:219], v3, s[20:21]
	global_load_dwordx4 v[28:31], v3, s[4:5] offset:1024
	global_load_dwordx4 v[76:79], v3, s[6:7] offset:1024
	global_load_dwordx4 v[124:127], v3, s[16:17] offset:1024
	global_load_dwordx4 v[172:175], v3, s[18:19] offset:1024
	global_load_dwordx4 v[220:223], v3, s[20:21] offset:1024
	global_load_dwordx4 v[32:35], v3, s[4:5] offset:2048
	global_load_dwordx4 v[80:83], v3, s[6:7] offset:2048
	global_load_dwordx4 v[128:131], v3, s[16:17] offset:2048
	global_load_dwordx4 v[176:179], v3, s[18:19] offset:2048
	global_load_dwordx4 v[224:227], v3, s[20:21] offset:2048
	global_load_dwordx4 v[36:39], v3, s[4:5] offset:3072
	global_load_dwordx4 v[84:87], v3, s[6:7] offset:3072
	global_load_dwordx4 v[132:135], v3, s[16:17] offset:3072
	global_load_dwordx4 v[180:183], v3, s[18:19] offset:3072
	global_load_dwordx4 v[228:231], v3, s[20:21] offset:3072
	global_load_dwordx4 v[40:43], v4, s[4:5]
	global_load_dwordx4 v[88:91], v4, s[6:7]
	global_load_dwordx4 v[136:139], v4, s[16:17]
	global_load_dwordx4 v[184:187], v4, s[18:19]
	global_load_dwordx4 v[232:235], v4, s[20:21]
	global_load_dwordx4 v[44:47], v4, s[4:5] offset:1024
	global_load_dwordx4 v[92:95], v4, s[6:7] offset:1024
	global_load_dwordx4 v[140:143], v4, s[16:17] offset:1024
	global_load_dwordx4 v[188:191], v4, s[18:19] offset:1024
	global_load_dwordx4 v[236:239], v4, s[20:21] offset:1024
	global_load_dwordx4 v[48:51], v4, s[4:5] offset:2048
	global_load_dwordx4 v[96:99], v4, s[6:7] offset:2048
	global_load_dwordx4 v[144:147], v4, s[16:17] offset:2048
	global_load_dwordx4 v[192:195], v4, s[18:19] offset:2048
	global_load_dwordx4 v[240:243], v4, s[20:21] offset:2048
	global_load_dwordx4 v[52:55], v4, s[4:5] offset:3072
	global_load_dwordx4 v[100:103], v4, s[6:7] offset:3072
	global_load_dwordx4 v[148:151], v4, s[16:17] offset:3072
	global_load_dwordx4 v[196:199], v4, s[18:19] offset:3072
	global_load_dwordx4 v[244:247], v4, s[20:21] offset:3072
	s_waitcnt vmcnt(58)
	v_mfma_f32_32x32x16_bf16 a[0:15], v[8:11], v[56:59], 0
	s_waitcnt vmcnt(57)
	v_mfma_f32_32x32x16_bf16 a[0:15], v[8:11], v[104:107], a[0:15]
	s_waitcnt vmcnt(56)
	v_mfma_f32_32x32x16_bf16 a[0:15], v[8:11], v[152:155], a[0:15]
	s_waitcnt vmcnt(55)
	v_mfma_f32_32x32x16_bf16 a[0:15], v[8:11], v[200:203], a[0:15]
	s_waitcnt vmcnt(53)
	v_mfma_f32_32x32x16_bf16 a[0:15], v[12:15], v[60:63], a[0:15]
	s_waitcnt vmcnt(52)
	v_mfma_f32_32x32x16_bf16 a[0:15], v[12:15], v[108:111], a[0:15]
	s_waitcnt vmcnt(51)
	v_mfma_f32_32x32x16_bf16 a[0:15], v[12:15], v[156:159], a[0:15]
	s_waitcnt vmcnt(50)
	v_mfma_f32_32x32x16_bf16 a[0:15], v[12:15], v[204:207], a[0:15]
	v_add_f32_e32 v8, 0, v248
	v_add_f32_e32 v8, v8, v249
	v_add_f32_e32 v8, v8, v250
	v_add_f32_e32 v8, v8, v251
	v_mov_b32_e32 v9, 0x3fb8aa3b
	s_waitcnt lgkmcnt(0)
	v_mul_f32_e32 v9, s22, v9
	v_exp_f32_e32 v9, v9
	v_add_f32_e32 v10, 0x2b8cbccc, v8
	v_div_scale_f32 v11, s[8:9], v10, v10, v9
	v_rcp_f32_e32 v12, v11
	v_div_scale_f32 v13, vcc, v9, v10, v9
	v_fma_f32 v14, -v11, v12, 1.0
	v_fmac_f32_e32 v12, v14, v12
	v_mul_f32_e32 v14, v13, v12
	v_fma_f32 v15, -v11, v14, v13
	v_fmac_f32_e32 v14, v15, v12
	v_fma_f32 v11, -v11, v14, v13
	v_div_fmas_f32 v11, v11, v12, v14
	v_div_fixup_f32 v9, v11, v10, v9
	v_lshlrev_b32_e32 v10, 2, v0
	v_add_u32_e32 v10, 0x4000, v10
	v_cmp_gt_u32_e32 vcc, 32, v0
	s_and_saveexec_b64 s[8:9], vcc
	ds_write2_b32 v10, v8, v9 offset0:128 offset1:160
	s_mov_b64 exec, s[8:9]
	s_waitcnt vmcnt(48)
	v_mfma_f32_32x32x16_bf16 a[0:15], v[16:19], v[64:67], a[0:15]
	s_waitcnt vmcnt(47)
	v_mfma_f32_32x32x16_bf16 a[0:15], v[16:19], v[112:115], a[0:15]
	s_waitcnt vmcnt(46)
	v_mfma_f32_32x32x16_bf16 a[0:15], v[16:19], v[160:163], a[0:15]
	s_waitcnt vmcnt(45)
	v_mfma_f32_32x32x16_bf16 a[0:15], v[16:19], v[208:211], a[0:15]
	s_waitcnt vmcnt(43)
	v_mfma_f32_32x32x16_bf16 a[0:15], v[20:23], v[68:71], a[0:15]
	s_waitcnt vmcnt(42)
	v_mfma_f32_32x32x16_bf16 a[0:15], v[20:23], v[116:119], a[0:15]
	s_waitcnt vmcnt(41)
	v_mfma_f32_32x32x16_bf16 a[0:15], v[20:23], v[164:167], a[0:15]
	s_waitcnt vmcnt(40)
	v_mfma_f32_32x32x16_bf16 a[0:15], v[20:23], v[212:215], a[0:15]
	s_waitcnt vmcnt(38)
	v_mfma_f32_32x32x16_bf16 a[0:15], v[24:27], v[72:75], a[0:15]
	s_waitcnt vmcnt(37)
	v_mfma_f32_32x32x16_bf16 a[0:15], v[24:27], v[120:123], a[0:15]
	s_waitcnt vmcnt(36)
	v_mfma_f32_32x32x16_bf16 a[0:15], v[24:27], v[168:171], a[0:15]
	s_waitcnt vmcnt(35)
	v_mfma_f32_32x32x16_bf16 a[0:15], v[24:27], v[216:219], a[0:15]
	s_waitcnt vmcnt(33)
	v_mfma_f32_32x32x16_bf16 a[0:15], v[28:31], v[76:79], a[0:15]
	s_waitcnt vmcnt(32)
	v_mfma_f32_32x32x16_bf16 a[0:15], v[28:31], v[124:127], a[0:15]
	s_waitcnt vmcnt(31)
	v_mfma_f32_32x32x16_bf16 a[0:15], v[28:31], v[172:175], a[0:15]
	s_waitcnt vmcnt(30)
	v_mfma_f32_32x32x16_bf16 a[0:15], v[28:31], v[220:223], a[0:15]
	s_waitcnt vmcnt(28)
	v_mfma_f32_32x32x16_bf16 a[0:15], v[32:35], v[80:83], a[0:15]
	s_waitcnt vmcnt(27)
	v_mfma_f32_32x32x16_bf16 a[0:15], v[32:35], v[128:131], a[0:15]
	s_waitcnt vmcnt(26)
	v_mfma_f32_32x32x16_bf16 a[0:15], v[32:35], v[176:179], a[0:15]
	s_waitcnt vmcnt(25)
	v_mfma_f32_32x32x16_bf16 a[0:15], v[32:35], v[224:227], a[0:15]
	s_waitcnt vmcnt(23)
	v_mfma_f32_32x32x16_bf16 a[0:15], v[36:39], v[84:87], a[0:15]
	s_waitcnt vmcnt(22)
	v_mfma_f32_32x32x16_bf16 a[0:15], v[36:39], v[132:135], a[0:15]
	s_waitcnt vmcnt(21)
	v_mfma_f32_32x32x16_bf16 a[0:15], v[36:39], v[180:183], a[0:15]
	s_waitcnt vmcnt(20)
	v_mfma_f32_32x32x16_bf16 a[0:15], v[36:39], v[228:231], a[0:15]
	s_waitcnt vmcnt(18)
	v_mfma_f32_32x32x16_bf16 a[0:15], v[40:43], v[88:91], a[0:15]
	s_waitcnt vmcnt(17)
	v_mfma_f32_32x32x16_bf16 a[0:15], v[40:43], v[136:139], a[0:15]
	s_waitcnt vmcnt(16)
	v_mfma_f32_32x32x16_bf16 a[0:15], v[40:43], v[184:187], a[0:15]
	s_waitcnt vmcnt(15)
	v_mfma_f32_32x32x16_bf16 a[0:15], v[40:43], v[232:235], a[0:15]
	s_waitcnt vmcnt(13)
	v_mfma_f32_32x32x16_bf16 a[0:15], v[44:47], v[92:95], a[0:15]
	s_waitcnt vmcnt(12)
	v_mfma_f32_32x32x16_bf16 a[0:15], v[44:47], v[140:143], a[0:15]
	s_waitcnt vmcnt(11)
	v_mfma_f32_32x32x16_bf16 a[0:15], v[44:47], v[188:191], a[0:15]
	s_waitcnt vmcnt(10)
	v_mfma_f32_32x32x16_bf16 a[0:15], v[44:47], v[236:239], a[0:15]
	s_waitcnt vmcnt(8)
	v_mfma_f32_32x32x16_bf16 a[0:15], v[48:51], v[96:99], a[0:15]
	s_waitcnt vmcnt(7)
	v_mfma_f32_32x32x16_bf16 a[0:15], v[48:51], v[144:147], a[0:15]
	s_waitcnt vmcnt(6)
	v_mfma_f32_32x32x16_bf16 a[0:15], v[48:51], v[192:195], a[0:15]
	s_waitcnt vmcnt(5)
	v_mfma_f32_32x32x16_bf16 a[0:15], v[48:51], v[240:243], a[0:15]
	v_mul_u32_u24_e32 v1, 0x1080, v1
	s_movk_i32 s4, 0x7f
	s_movk_i32 s6, 0x84
	v_cmp_lt_u32_e32 vcc, s4, v0
	v_lshrrev_b32_e32 v11, 3, v0
	v_and_b32_e32 v10, 31, v0
	v_and_b32_e32 v11, 4, v11
	v_mul_u32_u24_e32 v11, 0x84, v11
	v_lshlrev_b32_e32 v9, 2, v10
	v_bfe_u32 v6, v0, 2, 5
	v_and_b32_e32 v7, 3, v0
	v_add3_u32 v1, v1, v11, v9
	v_lshlrev_b32_e32 v8, 3, v7
	s_waitcnt vmcnt(3)
	v_mfma_f32_32x32x16_bf16 a[0:15], v[52:55], v[100:103], a[0:15]
	s_waitcnt vmcnt(2)
	v_mfma_f32_32x32x16_bf16 a[0:15], v[52:55], v[148:151], a[0:15]
	s_waitcnt vmcnt(1)
	v_mfma_f32_32x32x16_bf16 a[0:15], v[52:55], v[196:199], a[0:15]
	s_waitcnt vmcnt(0)
	v_mfma_f32_32x32x16_bf16 a[0:15], v[52:55], v[244:247], a[0:15]
	s_nop 11
	ds_write_b32 v1, a0
	ds_write_b32 v1, a1 offset:132
	ds_write_b32 v1, a2 offset:264
	ds_write_b32 v1, a3 offset:396
	ds_write_b32 v1, a4 offset:1056
	ds_write_b32 v1, a5 offset:1188
	ds_write_b32 v1, a6 offset:1320
	ds_write_b32 v1, a7 offset:1452
	ds_write_b32 v1, a8 offset:2112
	ds_write_b32 v1, a9 offset:2244
	ds_write_b32 v1, a10 offset:2376
	ds_write_b32 v1, a11 offset:2508
	ds_write_b32 v1, a12 offset:3168
	ds_write_b32 v1, a13 offset:3300
	ds_write_b32 v1, a14 offset:3432
	ds_write_b32 v1, a15 offset:3564
	v_lshlrev_b32_e32 v1, 2, v6
	s_waitcnt lgkmcnt(0)
	s_barrier
	s_and_saveexec_b64 s[4:5], vcc
	s_xor_b64 s[4:5], exec, s[4:5]
	s_cbranch_execz .LBB1_4
	v_mad_u32_u24 v5, v8, s6, v1
	ds_read_b32 v2, v5
	ds_read_b32 v4, v5 offset:4224
	ds_read_b32 v3, v5 offset:8448
	ds_read_b32 v5, v5 offset:12672
	s_waitcnt lgkmcnt(0)
	v_pk_add_f32 v[2:3], v[2:3], v[4:5]
	s_nop 0
	v_add_f32_e32 v3, v2, v3

	.amdhsa_kernel _Z13logits_kernelPKDv8_DF16bS1_PKfS3_PDv2_fS5_Pf
		.amdhsa_group_segment_fixed_size 17152
		.amdhsa_private_segment_fixed_size 0
		.amdhsa_kernarg_size 56
		.amdhsa_user_sgpr_count 2
		.amdhsa_user_sgpr_dispatch_ptr 0
		.amdhsa_user_sgpr_queue_ptr 0
		.amdhsa_user_sgpr_kernarg_segment_ptr 1
		.amdhsa_user_sgpr_dispatch_id 0
		.amdhsa_user_sgpr_kernarg_preload_length 0
		.amdhsa_user_sgpr_kernarg_preload_offset 0
		.amdhsa_user_sgpr_private_segment_size 0
		.amdhsa_uses_dynamic_stack 0
		.amdhsa_enable_private_segment 0
		.amdhsa_system_sgpr_workgroup_id_x 1
		.amdhsa_system_sgpr_workgroup_id_y 0
		.amdhsa_system_sgpr_workgroup_id_z 0
		.amdhsa_system_sgpr_workgroup_info 0
		.amdhsa_system_vgpr_workitem_id 0
		.amdhsa_next_free_vgpr 268
		.amdhsa_next_free_sgpr 23
		.amdhsa_accum_offset 252
		.amdhsa_reserve_vcc 1
		.amdhsa_float_round_mode_32 0
		.amdhsa_float_round_mode_16_64 0
		.amdhsa_float_denorm_mode_32 3
		.amdhsa_float_denorm_mode_16_64 3
		.amdhsa_dx10_clamp 1
		.amdhsa_ieee_mode 1
		.amdhsa_fp16_overflow 0
		.amdhsa_tg_split 0
		.amdhsa_exception_fp_ieee_invalid_op 0
		.amdhsa_exception_fp_denorm_src 0
		.amdhsa_exception_fp_ieee_div_zero 0
		.amdhsa_exception_fp_ieee_overflow 0
		.amdhsa_exception_fp_ieee_underflow 0
		.amdhsa_exception_fp_ieee_inexact 0
		.amdhsa_exception_int_div_zero 0
	.end_amdhsa_kernel

amdhsa.kernels:
  - .agpr_count:     0
    .args:
      - .actual_access:  read_only
        .address_space:  global
        .offset:         0
        .size:           8
        .value_kind:     global_buffer
      - .actual_access:  read_only
        .address_space:  global
        .offset:         8
        .size:           8
        .value_kind:     global_buffer
      - .actual_access:  read_only
        .address_space:  global
        .offset:         16
        .size:           8
        .value_kind:     global_buffer
      - .actual_access:  write_only
        .address_space:  global
        .offset:         24
        .size:           8
        .value_kind:     global_buffer
      - .actual_access:  write_only
        .address_space:  global
        .offset:         32
        .size:           8
        .value_kind:     global_buffer
      - .actual_access:  write_only
        .address_space:  global
        .offset:         40
        .size:           8
        .value_kind:     global_buffer
    .group_segment_fixed_size: 100880
    .kernarg_segment_align: 8
    .kernarg_segment_size: 48
    .language:       OpenCL C
    .language_version:
      - 2
      - 0
    .max_flat_workgroup_size: 768
    .name:           _Z14seg_sum_kernelPKfS0_S0_PDv8_DF16bS2_Pf
    .private_segment_fixed_size: 0
    .sgpr_count:     42
    .sgpr_spill_count: 0
    .symbol:         _Z14seg_sum_kernelPKfS0_S0_PDv8_DF16bS2_Pf.kd
    .uniform_work_group_size: 1
    .uses_dynamic_stack: false
    .vgpr_count:     142
    .vgpr_spill_count: 0
    .wavefront_size: 64
  - .agpr_count:     16
    .args:
      - .actual_access:  read_only
        .address_space:  global
        .offset:         0
        .size:           8
        .value_kind:     global_buffer
      - .actual_access:  read_only
        .address_space:  global
        .offset:         8
        .size:           8
        .value_kind:     global_buffer
      - .actual_access:  read_only
        .address_space:  global
        .offset:         16
        .size:           8
        .value_kind:     global_buffer
      - .actual_access:  read_only
        .address_space:  global
        .offset:         24
        .size:           8
        .value_kind:     global_buffer
      - .actual_access:  write_only
        .address_space:  global
        .offset:         32
        .size:           8
        .value_kind:     global_buffer
      - .actual_access:  write_only
        .address_space:  global
        .offset:         40
        .size:           8
        .value_kind:     global_buffer
      - .actual_access:  write_only
        .address_space:  global
        .offset:         48
        .size:           8
        .value_kind:     global_buffer
    .group_segment_fixed_size: 17152
    .kernarg_segment_align: 8
    .kernarg_segment_size: 56
    .language:       OpenCL C
    .language_version:
      - 2
      - 0
    .max_flat_workgroup_size: 256
    .name:           _Z13logits_kernelPKDv8_DF16bS1_PKfS3_PDv2_fS5_Pf
    .private_segment_fixed_size: 0
    .sgpr_count:     29
    .sgpr_spill_count: 0
    .symbol:         _Z13logits_kernelPKDv8_DF16bS1_PKfS3_PDv2_fS5_Pf.kd
    .uniform_work_group_size: 1
    .uses_dynamic_stack: false
    .vgpr_count:     268
    .vgpr_spill_count: 0
    .wavefront_size: 64
  - .agpr_count:     0
    .args:
      - .actual_access:  read_only
        .address_space:  global
        .offset:         0
        .size:           8
        .value_kind:     global_buffer
      - .actual_access:  read_only
        .address_space:  global
        .offset:         8
        .size:           8
        .value_kind:     global_buffer
      - .actual_access:  read_only
        .address_space:  global
        .offset:         16
        .size:           8
        .value_kind:     global_buffer
      - .actual_access:  read_only
        .address_space:  global
        .offset:         24
        .size:           8
        .value_kind:     global_buffer
      - .actual_access:  write_only
        .address_space:  global
        .offset:         32
        .size:           8
        .value_kind:     global_buffer
    .group_segment_fixed_size: 128
    .kernarg_segment_align: 8
    .kernarg_segment_size: 40
    .language:       OpenCL C
    .language_version:
      - 2
      - 0
    .max_flat_workgroup_size: 1024
    .name:           _Z12final_kernelPKDv4_fS1_PKfS3_Pf
    .private_segment_fixed_size: 0
    .sgpr_count:     15
    .sgpr_spill_count: 0
    .symbol:         _Z12final_kernelPKDv4_fS1_PKfS3_Pf.kd
    .uniform_work_group_size: 1
    .uses_dynamic_stack: false
    .vgpr_count:     50
    .vgpr_spill_count: 0
    .wavefront_size: 64
